# MLA online softmax: running max only advanced (and accumulators rescaled) when a row max grows by more than 2^8 in the exponent domain, exact after final normalisation
# speedup vs baseline: 1.0194x; 1.0076x over previous
.LBB0_463:
	s_nop 9
	v_max3_f32 v206, v82, v66, s90
	v_max_f32_e32 v208, v83, v67
	v_max3_f32 v206, v206, v84, v68
	v_max3_f32 v208, v208, v85, v69
	v_max3_f32 v206, v206, v86, v70
	v_max3_f32 v208, v208, v87, v71
	v_max3_f32 v206, v206, v88, v72
	v_max3_f32 v208, v208, v89, v73
	v_max3_f32 v206, v206, v90, v74
	v_max3_f32 v208, v208, v91, v75
	v_max3_f32 v206, v206, v92, v76
	v_max3_f32 v208, v208, v93, v77
	v_max3_f32 v206, v206, v94, v78
	v_max3_f32 v208, v208, v95, v79
	v_max3_f32 v206, v206, v96, v80
	v_max3_f32 v208, v208, v97, v81
	v_max_f32_e32 v206, v206, v208
	ds_bpermute_b32 v208, v236, v206
	s_waitcnt lgkmcnt(0)
	v_max3_f32 v206, v207, v206, v208
	v_add_f32_e32 v208, 0x4299999a, v207
	v_cmp_gt_f32_e32 vcc, v206, v208
	s_cbranch_vccnz .Lmy_lazy_a
	v_mov_b32_e32 v206, v207
	s_branch .LBB0_465
.Lmy_lazy_a:
	v_sub_f32_e32 v207, v207, v206
	v_mul_f32_e32 v207, 0x3dd53b94, v207
	v_exp_f32_e32 v208, v207
	s_nop 0
	v_pk_mul_f32 v[64:65], v[64:65], v[208:209] op_sel_hi:[1,0]
	v_pk_mul_f32 v[62:63], v[62:63], v[208:209] op_sel_hi:[1,0]
	v_pk_mul_f32 v[60:61], v[60:61], v[208:209] op_sel_hi:[1,0]
	v_pk_mul_f32 v[58:59], v[58:59], v[208:209] op_sel_hi:[1,0]
	v_pk_mul_f32 v[56:57], v[56:57], v[208:209] op_sel_hi:[1,0]
	v_pk_mul_f32 v[54:55], v[54:55], v[208:209] op_sel_hi:[1,0]
	v_pk_mul_f32 v[52:53], v[52:53], v[208:209] op_sel_hi:[1,0]
	v_pk_mul_f32 v[50:51], v[50:51], v[208:209] op_sel_hi:[1,0]
	v_pk_mul_f32 v[48:49], v[48:49], v[208:209] op_sel_hi:[1,0]
	v_pk_mul_f32 v[46:47], v[46:47], v[208:209] op_sel_hi:[1,0]
	v_pk_mul_f32 v[44:45], v[44:45], v[208:209] op_sel_hi:[1,0]
	v_pk_mul_f32 v[42:43], v[42:43], v[208:209] op_sel_hi:[1,0]
	v_pk_mul_f32 v[40:41], v[40:41], v[208:209] op_sel_hi:[1,0]
	v_pk_mul_f32 v[38:39], v[38:39], v[208:209] op_sel_hi:[1,0]
	v_pk_mul_f32 v[36:37], v[36:37], v[208:209] op_sel_hi:[1,0]
	v_pk_mul_f32 v[34:35], v[34:35], v[208:209] op_sel_hi:[1,0]
	v_pk_mul_f32 v[32:33], v[32:33], v[208:209] op_sel_hi:[1,0]
	v_pk_mul_f32 v[30:31], v[30:31], v[208:209] op_sel_hi:[1,0]
	v_pk_mul_f32 v[28:29], v[28:29], v[208:209] op_sel_hi:[1,0]
	v_pk_mul_f32 v[26:27], v[26:27], v[208:209] op_sel_hi:[1,0]
	v_pk_mul_f32 v[24:25], v[24:25], v[208:209] op_sel_hi:[1,0]
	v_pk_mul_f32 v[22:23], v[22:23], v[208:209] op_sel_hi:[1,0]
	v_pk_mul_f32 v[20:21], v[20:21], v[208:209] op_sel_hi:[1,0]
	v_pk_mul_f32 v[18:19], v[18:19], v[208:209] op_sel_hi:[1,0]
	v_pk_mul_f32 v[16:17], v[16:17], v[208:209] op_sel_hi:[1,0]
	v_pk_mul_f32 v[14:15], v[14:15], v[208:209] op_sel_hi:[1,0]
	v_pk_mul_f32 v[12:13], v[12:13], v[208:209] op_sel_hi:[1,0]
	v_pk_mul_f32 v[10:11], v[10:11], v[208:209] op_sel_hi:[1,0]
	v_pk_mul_f32 v[8:9], v[8:9], v[208:209] op_sel_hi:[1,0]
	v_pk_mul_f32 v[6:7], v[6:7], v[208:209] op_sel_hi:[1,0]
	v_pk_mul_f32 v[4:5], v[4:5], v[208:209] op_sel_hi:[1,0]
	v_pk_mul_f32 v[2:3], v[2:3], v[208:209] op_sel_hi:[1,0]
	v_mul_f32_e32 v205, v205, v208

.LBB0_476:
	s_nop 9
	v_max3_f32 v207, v82, v66, s90
	v_max_f32_e32 v209, v83, v67
	v_max3_f32 v207, v207, v84, v68
	v_max3_f32 v209, v209, v85, v69
	v_max3_f32 v207, v207, v86, v70
	v_max3_f32 v209, v209, v87, v71
	v_max3_f32 v207, v207, v88, v72
	v_max3_f32 v209, v209, v89, v73
	v_max3_f32 v207, v207, v90, v74
	v_max3_f32 v209, v209, v91, v75
	v_max3_f32 v207, v207, v92, v76
	v_max3_f32 v209, v209, v93, v77
	v_max3_f32 v207, v207, v94, v78
	v_max3_f32 v209, v209, v95, v79
	v_max3_f32 v207, v207, v96, v80
	v_max3_f32 v209, v209, v97, v81
	v_max_f32_e32 v207, v207, v209
	ds_bpermute_b32 v209, v1, v207
	s_waitcnt lgkmcnt(0)
	v_max3_f32 v207, v208, v207, v209
	v_add_f32_e32 v209, 0x4299999a, v208
	v_cmp_gt_f32_e32 vcc, v207, v209
	s_cbranch_vccnz .Lmy_lazy_b
	v_mov_b32_e32 v207, v208
	s_branch .LBB0_478
.Lmy_lazy_b:
	v_sub_f32_e32 v208, v208, v207
	v_mul_f32_e32 v208, 0x3dd53b94, v208
	v_exp_f32_e32 v208, v208
	s_nop 0
	v_pk_mul_f32 v[64:65], v[64:65], v[208:209] op_sel_hi:[1,0]
	v_pk_mul_f32 v[62:63], v[62:63], v[208:209] op_sel_hi:[1,0]
	v_pk_mul_f32 v[60:61], v[60:61], v[208:209] op_sel_hi:[1,0]
	v_pk_mul_f32 v[58:59], v[58:59], v[208:209] op_sel_hi:[1,0]
	v_pk_mul_f32 v[56:57], v[56:57], v[208:209] op_sel_hi:[1,0]
	v_pk_mul_f32 v[54:55], v[54:55], v[208:209] op_sel_hi:[1,0]
	v_pk_mul_f32 v[52:53], v[52:53], v[208:209] op_sel_hi:[1,0]
	v_pk_mul_f32 v[50:51], v[50:51], v[208:209] op_sel_hi:[1,0]
	v_pk_mul_f32 v[48:49], v[48:49], v[208:209] op_sel_hi:[1,0]
	v_pk_mul_f32 v[46:47], v[46:47], v[208:209] op_sel_hi:[1,0]
	v_pk_mul_f32 v[44:45], v[44:45], v[208:209] op_sel_hi:[1,0]
	v_pk_mul_f32 v[42:43], v[42:43], v[208:209] op_sel_hi:[1,0]
	v_pk_mul_f32 v[40:41], v[40:41], v[208:209] op_sel_hi:[1,0]
	v_pk_mul_f32 v[38:39], v[38:39], v[208:209] op_sel_hi:[1,0]
	v_pk_mul_f32 v[36:37], v[36:37], v[208:209] op_sel_hi:[1,0]
	v_pk_mul_f32 v[34:35], v[34:35], v[208:209] op_sel_hi:[1,0]
	v_pk_mul_f32 v[32:33], v[32:33], v[208:209] op_sel_hi:[1,0]
	v_pk_mul_f32 v[30:31], v[30:31], v[208:209] op_sel_hi:[1,0]
	v_pk_mul_f32 v[28:29], v[28:29], v[208:209] op_sel_hi:[1,0]
	v_pk_mul_f32 v[26:27], v[26:27], v[208:209] op_sel_hi:[1,0]
	v_pk_mul_f32 v[24:25], v[24:25], v[208:209] op_sel_hi:[1,0]
	v_pk_mul_f32 v[22:23], v[22:23], v[208:209] op_sel_hi:[1,0]
	v_pk_mul_f32 v[20:21], v[20:21], v[208:209] op_sel_hi:[1,0]
	v_pk_mul_f32 v[18:19], v[18:19], v[208:209] op_sel_hi:[1,0]
	v_pk_mul_f32 v[16:17], v[16:17], v[208:209] op_sel_hi:[1,0]
	v_pk_mul_f32 v[14:15], v[14:15], v[208:209] op_sel_hi:[1,0]
	v_pk_mul_f32 v[12:13], v[12:13], v[208:209] op_sel_hi:[1,0]
	v_pk_mul_f32 v[10:11], v[10:11], v[208:209] op_sel_hi:[1,0]
	v_pk_mul_f32 v[8:9], v[8:9], v[208:209] op_sel_hi:[1,0]
	v_pk_mul_f32 v[6:7], v[6:7], v[208:209] op_sel_hi:[1,0]
	v_pk_mul_f32 v[4:5], v[4:5], v[208:209] op_sel_hi:[1,0]
	v_pk_mul_f32 v[2:3], v[2:3], v[208:209] op_sel_hi:[1,0]
	v_mul_f32_e32 v205, v205, v208
